# attention main loop: every 8-byte instruction placed on an 8-byte boundary (e32 to e64 promotions and s_nop padding)
# speedup vs baseline: 1.0029x; 1.0029x over previous
.LBB0_724:
	v_lshlrev_b32_e32 v32, 1, v118
	v_and_b32_e32 v218, 32, v32
	v_lshrrev_b32_e32 v32, 2, v118
	v_and_or_b32 v32, v32, 3, v236
	v_lshlrev_b32_e32 v217, 6, v32
	v_add_u32_e32 v32, 0, v218
	v_add3_u32 v239, v32, v216, v217
	v_max3_f32 v32, v16, v17, v0
	v_max3_f32 v33, v18, v19, v1
	s_and_b32 s19, s41, 0x3fffffc0
	v_max3_f32 v32, v32, v2, v3
	v_max3_f32 v33, v33, v22, v23
	s_add_i32 s20, s45, 0x100
	v_max3_f32 v32, v32, v20, v21
	v_max3_f32 v33, v33, v6, v7
	s_lshl_b32 s19, s19, 2
	v_max3_f32 v32, v32, v4, v5
	v_max3_f32 v33, v33, v26, v27
	s_lshr_b32 s39, s20, 6
	v_max3_f32 v32, v32, v24, v25
	v_max3_f32 v33, v33, v10, v11
	s_mov_b64 s[20:21], 0x60000
	v_max3_f32 v32, v32, v8, v9
	v_max3_f32 v33, v33, v30, v31
	s_add_i32 s19, s19, 0
	v_max3_f32 v32, v32, v28, v29
	v_max3_f32 v33, v33, v14, v15
	s_cmp_lg_u32 0, -1
	v_max3_f32 v32, v32, v12, v13
	s_mov_b32 s96, 1
	v_max_f32_e32 v32, v32, v33
	s_mov_b32 s22, 0
	v_mov_b32_e32 v33, v32
	s_nop 1
	v_permlane32_swap_b32_e32 v32, v33
	v_max_f32_e32 v32, v32, v33
	v_lshl_add_u32 v235, v214, 2, s19
	v_sub_f32_e32 v64, v0, v32
	v_sub_f32_e32 v0, v17, v32
	v_sub_f32_e32 v16, v16, v32
	v_sub_f32_e32 v65, v1, v32
	v_sub_f32_e32 v1, v18, v32
	v_sub_f32_e32 v66, v2, v32
	v_sub_f32_e32 v2, v19, v32
	s_nop 0
	v_exp_f32_e32 v81, v0
	v_lshl_add_u32 v0, v236, 2, 0
	v_sub_f32_e32 v67, v3, v32
	v_sub_f32_e32 v3, v20, v32
	v_sub_f32_e32 v68, v4, v32
	v_sub_f32_e32 v4, v21, v32
	v_sub_f32_e32 v69, v5, v32
	v_sub_f32_e32 v5, v22, v32
	v_sub_f32_e32 v70, v6, v32
	v_sub_f32_e32 v6, v23, v32
	v_sub_f32_e32 v71, v7, v32
	v_sub_f32_e32 v7, v24, v32
	v_sub_f32_e32 v72, v8, v32
	v_sub_f32_e32 v8, v25, v32
	v_sub_f32_e32 v73, v9, v32
	v_sub_f32_e32 v9, v26, v32
	v_sub_f32_e32 v74, v10, v32
	v_sub_f32_e32 v10, v27, v32
	v_sub_f32_e32 v75, v11, v32
	v_sub_f32_e32 v11, v28, v32
	v_sub_f32_e32 v76, v12, v32
	v_sub_f32_e32 v12, v29, v32
	v_sub_f32_e32 v77, v13, v32
	v_sub_f32_e32 v13, v30, v32
	v_sub_f32_e32 v78, v14, v32
	v_sub_f32_e32 v14, v31, v32
	v_add_u32_e32 v28, 0x15100, v0
	v_sub_f32_e32 v79, v15, v32
	v_exp_f32_e32 v80, v16
	v_exp_f32_e32 v82, v1
	v_exp_f32_e32 v83, v2
	v_exp_f32_e32 v84, v3
	v_exp_f32_e32 v85, v4
	v_exp_f32_e32 v86, v5
	v_exp_f32_e32 v87, v6
	v_exp_f32_e32 v88, v7
	v_exp_f32_e32 v89, v8
	v_exp_f32_e32 v90, v9
	v_exp_f32_e32 v91, v10
	v_exp_f32_e32 v92, v11
	v_exp_f32_e32 v93, v12
	v_exp_f32_e32 v94, v13
	v_exp_f32_e32 v95, v14
	ds_read_b128 v[0:3], v28
	ds_read_b128 v[4:7], v28 offset:32
	ds_read_b128 v[8:11], v28 offset:128
	ds_read_b128 v[12:15], v28 offset:160
	ds_read_b128 v[16:19], v28 offset:64
	ds_read_b128 v[20:23], v28 offset:96
	ds_read_b128 v[24:27], v28 offset:192
	ds_read_b128 v[28:31], v28 offset:224
	s_waitcnt vmcnt(0) lgkmcnt(0)
	s_barrier
	v_add_f32_e32 v202, v97, v32
	v_exp_f32_e32 v64, v64
	s_waitcnt lgkmcnt(7)
	v_pk_add_f32 v[48:49], v[202:203], v[0:1] op_sel_hi:[0,1] neg_lo:[1,0] neg_hi:[1,0]
	v_lshl_add_u64 v[0:1], v[114:115], 0, s[20:21]
	s_mov_b32 s20, m0
	s_mov_b32 m0, s30
	s_nop 0
	global_load_lds_dwordx4 v[0:1], off
	s_mov_b32 m0, s20
	s_mov_b64 s[20:21], 0x20000
	v_lshl_add_u64 v[0:1], v[116:117], 0, s[20:21]
	s_cselect_b32 s20, 0, 0
	s_add_i32 s18, s20, s18
	s_add_i32 s18, s18, 0x8000
	s_mov_b32 s20, m0
	s_mov_b32 m0, s18
	s_nop 0
	global_load_lds_dwordx4 v[0:1], off
	s_mov_b32 m0, s20
	ds_read_b128 v[158:161], v238 offset:8192
	ds_read_b128 v[146:149], v238 offset:8704
	ds_read_b128 v[154:157], v238 offset:10240
	ds_read_b128 v[142:145], v238 offset:10752
	ds_read_b128 v[150:153], v238 offset:12288
	ds_read_b128 v[138:141], v238 offset:12800
	ds_read_b128 v[134:137], v238 offset:14336
	ds_read_b128 v[130:133], v238 offset:14848
	v_exp_f32_e32 v65, v65
	v_exp_f32_e32 v66, v66
	v_exp_f32_e32 v67, v67
	v_exp_f32_e32 v68, v68
	v_exp_f32_e32 v69, v69
	v_exp_f32_e32 v70, v70
	v_exp_f32_e32 v71, v71
	v_exp_f32_e32 v72, v72
	v_exp_f32_e32 v73, v73
	v_exp_f32_e32 v74, v74
	v_exp_f32_e32 v75, v75
	v_exp_f32_e32 v76, v76
	v_exp_f32_e32 v77, v77
	v_exp_f32_e32 v78, v78
	v_exp_f32_e32 v79, v79
	s_waitcnt vmcnt(2) lgkmcnt(0)
	s_barrier
	v_and_b32_e32 v0, 3, v118
	s_waitcnt lgkmcnt(13)
	v_pk_add_f32 v[32:33], v[202:203], v[8:9] op_sel_hi:[0,1] neg_lo:[1,0] neg_hi:[1,0]
	v_pk_add_f32 v[50:51], v[202:203], v[2:3] op_sel_hi:[0,1] neg_lo:[1,0] neg_hi:[1,0]
	v_pk_add_f32 v[34:35], v[202:203], v[10:11] op_sel_hi:[0,1] neg_lo:[1,0] neg_hi:[1,0]
	v_pk_add_f32 v[52:53], v[202:203], v[4:5] op_sel_hi:[0,1] neg_lo:[1,0] neg_hi:[1,0]
	s_waitcnt lgkmcnt(12)
	v_pk_add_f32 v[36:37], v[202:203], v[12:13] op_sel_hi:[0,1] neg_lo:[1,0] neg_hi:[1,0]
	v_pk_add_f32 v[54:55], v[202:203], v[6:7] op_sel_hi:[0,1] neg_lo:[1,0] neg_hi:[1,0]
	v_pk_add_f32 v[38:39], v[202:203], v[14:15] op_sel_hi:[0,1] neg_lo:[1,0] neg_hi:[1,0]
	s_waitcnt lgkmcnt(11)
	v_pk_add_f32 v[56:57], v[202:203], v[16:17] op_sel_hi:[0,1] neg_lo:[1,0] neg_hi:[1,0]
	s_waitcnt lgkmcnt(9)
	v_pk_add_f32 v[40:41], v[202:203], v[24:25] op_sel_hi:[0,1] neg_lo:[1,0] neg_hi:[1,0]
	v_pk_add_f32 v[58:59], v[202:203], v[18:19] op_sel_hi:[0,1] neg_lo:[1,0] neg_hi:[1,0]
	v_pk_add_f32 v[42:43], v[202:203], v[26:27] op_sel_hi:[0,1] neg_lo:[1,0] neg_hi:[1,0]
	v_pk_add_f32 v[60:61], v[202:203], v[20:21] op_sel_hi:[0,1] neg_lo:[1,0] neg_hi:[1,0]
	s_waitcnt lgkmcnt(8)
	v_pk_add_f32 v[44:45], v[202:203], v[28:29] op_sel_hi:[0,1] neg_lo:[1,0] neg_hi:[1,0]
	v_pk_add_f32 v[62:63], v[202:203], v[22:23] op_sel_hi:[0,1] neg_lo:[1,0] neg_hi:[1,0]
	v_pk_add_f32 v[46:47], v[202:203], v[30:31] op_sel_hi:[0,1] neg_lo:[1,0] neg_hi:[1,0]
	s_andn2_b64 vcc, exec, s[2:3]
	v_cmp_gt_u32_e64 s[2:3], 32, v199
	v_lshl_add_u32 v219, v236, 2, s19
	v_lshlrev_b32_e32 v204, 4, v0
	s_cbranch_vccnz .LBB0_742
	s_lshl_b64 s[18:19], s[4:5], 1
	s_add_u32 s18, s70, s18
	s_addc_u32 s19, s71, s19
	s_add_u32 s18, s18, s14
	s_addc_u32 s19, s19, s15
	v_lshl_add_u64 v[206:207], s[18:19], 0, v[96:97]
	s_lshl_b64 s[18:19], s[16:17], 1
	s_add_u32 s18, s18, s14
	v_mov_b32_e32 v205, v97
	s_addc_u32 s19, s19, s15
	v_lshl_add_u64 v[0:1], s[18:19], 0, v[204:205]
	s_lshl_b32 s18, s41, 9
	s_and_b32 s18, s18, 0x18000
	v_lshl_or_b32 v2, v241, 11, s18
	v_mov_b32_e32 v3, v97
	v_lshl_add_u64 v[0:1], v[0:1], 0, v[2:3]
	v_mov_b32_e32 v16, v97
	v_mov_b32_e32 v17, v97
	v_lshl_add_u64 v[208:209], s[70:71], 0, v[0:1]
	v_subrev_u32_e32 v245, s14, v0
	v_add_u32_e32 v245, 0x7fc0000, v245
	v_lshl_add_u32 v244, s4, 1, v96
	s_add_u32 s98, s70, s14
	s_addc_u32 s99, s71, s15
	s_add_u32 s98, s98, s12
	s_addc_u32 s99, s99, s13
	s_add_u32 s98, s98, 0x16e80000
	s_addc_u32 s99, s99, 0
	v_readlane_b32 s18, v253, 11
	v_mov_b32_e32 v18, v97
	v_mov_b32_e32 v19, v97
	v_mov_b32_e32 v20, v97
	v_mov_b32_e32 v21, v97
	v_mov_b32_e32 v22, v97
	v_mov_b32_e32 v23, v97
	v_mov_b32_e32 v24, v97
	v_mov_b32_e32 v25, v97
	v_mov_b32_e32 v26, v97
	v_mov_b32_e32 v27, v97
	v_mov_b32_e32 v28, v97
	v_mov_b32_e32 v29, v97
	v_mov_b32_e32 v30, v97
	v_mov_b32_e32 v31, v97
	v_mov_b64_e32 v[0:1], v[16:17]
	v_lshl_add_u32 v205, v215, 4, s18
	s_mov_b32 s18, 0
	s_movk_i32 s22, 0x4000
	s_movk_i32 s38, 0x2000
	v_mov_b32_e32 v240, 0
	s_mov_b32 s23, 6
	v_mov_b64_e32 v[2:3], v[18:19]
	v_mov_b64_e32 v[4:5], v[20:21]
	v_mov_b64_e32 v[6:7], v[22:23]
	v_mov_b64_e32 v[8:9], v[24:25]
	v_mov_b64_e32 v[10:11], v[26:27]
	v_mov_b64_e32 v[12:13], v[28:29]
	v_mov_b64_e32 v[14:15], v[30:31]
	s_nop 0
.LBB0_726:
	v_add_u32_e64 v164, s18, v239
	s_add_i32 s18, s38, s30
	s_mov_b32 s19, m0
	s_mov_b32 m0, s18
	s_nop 0
	global_load_lds_dwordx4 v244, s[98:99]
	s_mov_b32 m0, s19
	s_add_i32 s18, s22, s31
	s_mov_b32 s19, m0
	s_mov_b32 m0, s18
	s_nop 0
	s_nop 0
	global_load_lds_dwordx4 v245, s[98:99]
	s_mov_b32 m0, s19
	s_nop 0
	s_add_u32 s98, s98, 0x20000
	s_addc_u32 s99, s99, 0
	s_nop 0
	ds_read_b64_tr_b16 v[190:191], v164 offset:24576
	ds_read_b64_tr_b16 v[192:193], v164 offset:25088
	s_waitcnt lgkmcnt(2)
	s_nop 0
	v_mfma_f32_32x32x16_bf16 v[48:63], v[158:161], v[110:113], v[48:63]
	v_add_f32_e32 v114, v80, v81
	v_add_f32_e32 v114, v82, v114
	v_add_f32_e32 v114, v83, v114
	v_add_f32_e32 v114, v84, v114
	v_add_f32_e64 v114, v85, v114
	v_cvt_pk_bf16_f32 v126, v80, v81
	v_cvt_pk_bf16_f32 v127, v82, v83
	ds_read_b64_tr_b16 v[186:187], v164 offset:28672
	ds_read_b64_tr_b16 v[188:189], v164 offset:29184
	v_mfma_f32_32x32x16_bf16 v[32:47], v[146:149], v[110:113], v[32:47]
	v_add_f32_e32 v80, v86, v114
	v_add_f32_e32 v80, v87, v80
	v_add_f32_e32 v80, v88, v80
	v_add_f32_e32 v80, v89, v80
	v_cvt_pk_bf16_f32 v128, v84, v85
	v_cvt_pk_bf16_f32 v129, v86, v87
	ds_read_b64_tr_b16 v[182:183], v164 offset:25600
	ds_read_b64_tr_b16 v[184:185], v164 offset:26112
	v_mfma_f32_32x32x16_bf16 v[48:63], v[154:157], v[106:109], v[48:63]
	v_add_f32_e32 v80, v90, v80
	v_add_f32_e32 v80, v91, v80
	v_add_f32_e32 v80, v92, v80
	v_add_f32_e32 v80, v93, v80
	v_cvt_pk_bf16_f32 v122, v88, v89
	v_cvt_pk_bf16_f32 v123, v90, v91
	ds_read_b64_tr_b16 v[178:179], v164 offset:29696
	ds_read_b64_tr_b16 v[180:181], v164 offset:30208
	v_mfma_f32_32x32x16_bf16 v[32:47], v[142:145], v[106:109], v[32:47]
	v_add_f32_e32 v80, v94, v80
	v_add_f32_e32 v80, v95, v80
	v_add_f32_e32 v80, v64, v80
	v_add_f32_e32 v80, v65, v80
	v_cvt_pk_bf16_f32 v124, v92, v93
	v_cvt_pk_bf16_f32 v125, v94, v95
	ds_read_b64_tr_b16 v[166:167], v164 offset:26624
	ds_read_b64_tr_b16 v[168:169], v164 offset:27136
	v_mfma_f32_32x32x16_bf16 v[48:63], v[150:153], v[102:105], v[48:63]
	v_add_f32_e32 v80, v66, v80
	v_add_f32_e32 v80, v67, v80
	v_add_f32_e32 v80, v68, v80
	v_add_f32_e32 v80, v69, v80
	v_cvt_pk_bf16_f32 v118, v64, v65
	v_cvt_pk_bf16_f32 v119, v66, v67
	ds_read_b64_tr_b16 v[174:175], v164 offset:30720
	ds_read_b64_tr_b16 v[176:177], v164 offset:31232
	v_mfma_f32_32x32x16_bf16 v[32:47], v[138:141], v[102:105], v[32:47]
	v_add_f32_e32 v64, v70, v80
	v_add_f32_e32 v64, v71, v64
	v_add_f32_e32 v64, v72, v64
	v_add_f32_e32 v64, v73, v64
	v_cvt_pk_bf16_f32 v120, v68, v69
	v_cvt_pk_bf16_f32 v121, v70, v71
	ds_read_b64_tr_b16 v[170:171], v164 offset:27648
	ds_read_b64_tr_b16 v[172:173], v164 offset:28160
	v_mfma_f32_32x32x16_bf16 v[48:63], v[134:137], v[98:101], v[48:63]
	v_add_f32_e32 v64, v74, v64
	v_add_f32_e32 v64, v75, v64
	v_add_f32_e32 v64, v76, v64
	v_add_f32_e32 v64, v77, v64
	v_cvt_pk_bf16_f32 v114, v72, v73
	v_cvt_pk_bf16_f32 v115, v74, v75
	ds_read_b64_tr_b16 v[162:163], v164 offset:31744
	ds_read_b64_tr_b16 v[164:165], v164 offset:32256
	v_mfma_f32_32x32x16_bf16 v[32:47], v[130:133], v[98:101], v[32:47]
	v_add_f32_e32 v64, v78, v64
	v_add_f32_e32 v64, v79, v64
	v_add_f32_e64 v224, v240, v64
	v_cvt_pk_bf16_f32 v116, v76, v77
	v_cvt_pk_bf16_f32 v117, v78, v79
	s_waitcnt lgkmcnt(14)
	s_nop 0
	ds_read_b128 v[64:67], v205
	ds_read_b128 v[68:71], v205 offset:32
	ds_read_b128 v[82:85], v205 offset:128
	ds_read_b128 v[86:89], v205 offset:160
	ds_read_b128 v[72:75], v205 offset:64
	ds_read_b128 v[76:79], v205 offset:96
	ds_read_b128 v[90:93], v205 offset:192
	ds_read_b128 v[138:141], v205 offset:224
	v_max_f32_e64 v80, v48, v49
	v_max3_f32 v81, v50, v51, v33
	v_max3_f32 v80, v80, v32, v34
	v_max3_f32 v80, v80, v35, v52
	v_max3_f32 v81, v81, v54, v55
	v_max3_f32 v80, v80, v53, v36
	v_max3_f32 v81, v81, v38, v39
	v_max3_f32 v80, v80, v37, v56
	v_max3_f32 v81, v81, v58, v59
	v_max3_f32 v80, v80, v57, v40
	v_max3_f32 v81, v81, v42, v43
	v_max3_f32 v80, v80, v41, v60
	v_max3_f32 v81, v81, v62, v63
	v_max3_f32 v80, v80, v61, v44
	v_max3_f32 v81, v81, v46, v47
	v_max3_f32 v80, v80, v45, v81
	v_mov_b32_e32 v81, v80
	s_nop 1
	v_permlane32_swap_b32_e32 v80, v81
	v_max_f32_e32 v80, v80, v81
	v_cmp_lt_f32_e32 vcc, s51, v80
	s_cmp_lg_u64 vcc, 0
	s_cselect_b64 s[18:19], -1, 0
	s_cbranch_vccnz .LBB0_734
.LBB0_727:
	v_mfma_f32_32x32x16_bf16 v[16:31], v[126:129], v[190:193], v[16:31]
	v_exp_f32_e32 v48, v48
	v_exp_f32_e32 v49, v49
	v_exp_f32_e64 v50, v50
	v_exp_f32_e32 v51, v51
	s_waitcnt lgkmcnt(14)
	v_mfma_f32_32x32x16_bf16 v[0:15], v[126:129], v[186:189], v[0:15]
	v_exp_f32_e32 v52, v52
	v_exp_f32_e32 v53, v53
	v_exp_f32_e32 v54, v54
	v_exp_f32_e32 v55, v55
	v_add_u32_e64 v80, s22, v238
	ds_read_b128 v[134:137], v80
	ds_read_b128 v[130:133], v80 offset:512
	v_mfma_f32_32x32x16_bf16 v[16:31], v[122:125], v[182:185], v[16:31]
	v_exp_f32_e32 v56, v56
	v_exp_f32_e32 v57, v57
	v_exp_f32_e32 v58, v58
	v_exp_f32_e32 v59, v59
	ds_read_b128 v[146:149], v80 offset:2048
	ds_read_b128 v[142:145], v80 offset:2560
	v_mfma_f32_32x32x16_bf16 v[0:15], v[122:125], v[178:181], v[0:15]
	v_exp_f32_e32 v60, v60
	v_exp_f32_e32 v61, v61
	v_exp_f32_e32 v62, v62
	v_exp_f32_e32 v63, v63
	ds_read_b128 v[158:161], v80 offset:4096
	ds_read_b128 v[154:157], v80 offset:4608
	v_mfma_f32_32x32x16_bf16 v[16:31], v[118:121], v[166:169], v[16:31]
	v_exp_f32_e32 v32, v32
	v_exp_f32_e32 v33, v33
	v_exp_f32_e32 v34, v34
	v_exp_f32_e32 v35, v35
	ds_read_b128 v[166:169], v80 offset:6144
	ds_read_b128 v[150:153], v80 offset:6656
	s_waitcnt lgkmcnt(14)
	s_nop 0
	v_mfma_f32_32x32x16_bf16 v[0:15], v[118:121], v[174:177], v[0:15]
	v_exp_f32_e32 v36, v36
	v_exp_f32_e32 v37, v37
	v_exp_f32_e32 v38, v38
	v_exp_f32_e32 v39, v39
	v_mfma_f32_32x32x16_bf16 v[16:31], v[114:117], v[170:173], v[16:31]
	v_exp_f32_e32 v40, v40
	v_exp_f32_e32 v41, v41
	v_exp_f32_e32 v42, v42
	v_exp_f32_e32 v43, v43
	v_mfma_f32_32x32x16_bf16 v[0:15], v[114:117], v[162:165], v[0:15]
	v_exp_f32_e32 v44, v44
	v_exp_f32_e32 v45, v45
	v_exp_f32_e64 v46, v46
	v_exp_f32_e32 v47, v47
	s_waitcnt vmcnt(2) lgkmcnt(0)
	v_pk_add_f32 v[80:81], v[64:65], v[202:203] op_sel_hi:[1,0] neg_lo:[0,1] neg_hi:[0,1]
	v_pk_add_f32 v[64:65], v[82:83], v[202:203] op_sel_hi:[1,0] neg_lo:[0,1] neg_hi:[0,1]
	v_pk_add_f32 v[82:83], v[66:67], v[202:203] op_sel_hi:[1,0] neg_lo:[0,1] neg_hi:[0,1]
	v_pk_add_f32 v[66:67], v[84:85], v[202:203] op_sel_hi:[1,0] neg_lo:[0,1] neg_hi:[0,1]
	v_pk_add_f32 v[84:85], v[68:69], v[202:203] op_sel_hi:[1,0] neg_lo:[0,1] neg_hi:[0,1]
	v_pk_add_f32 v[68:69], v[86:87], v[202:203] op_sel_hi:[1,0] neg_lo:[0,1] neg_hi:[0,1]
	v_pk_add_f32 v[86:87], v[70:71], v[202:203] op_sel_hi:[1,0] neg_lo:[0,1] neg_hi:[0,1]
	v_pk_add_f32 v[70:71], v[88:89], v[202:203] op_sel_hi:[1,0] neg_lo:[0,1] neg_hi:[0,1]
	v_pk_add_f32 v[88:89], v[72:73], v[202:203] op_sel_hi:[1,0] neg_lo:[0,1] neg_hi:[0,1]
	v_pk_add_f32 v[72:73], v[90:91], v[202:203] op_sel_hi:[1,0] neg_lo:[0,1] neg_hi:[0,1]
	v_pk_add_f32 v[90:91], v[74:75], v[202:203] op_sel_hi:[1,0] neg_lo:[0,1] neg_hi:[0,1]
	v_pk_add_f32 v[74:75], v[92:93], v[202:203] op_sel_hi:[1,0] neg_lo:[0,1] neg_hi:[0,1]
	v_pk_add_f32 v[92:93], v[76:77], v[202:203] op_sel_hi:[1,0] neg_lo:[0,1] neg_hi:[0,1]
	v_pk_add_f32 v[76:77], v[138:139], v[202:203] op_sel_hi:[1,0] neg_lo:[0,1] neg_hi:[0,1]
	v_pk_add_f32 v[94:95], v[78:79], v[202:203] op_sel_hi:[1,0] neg_lo:[0,1] neg_hi:[0,1]
	v_pk_add_f32 v[78:79], v[140:141], v[202:203] op_sel_hi:[1,0] neg_lo:[0,1] neg_hi:[0,1]
	s_barrier
	s_andn2_b64 vcc, exec, s[18:19]
	s_cbranch_vccnz .LBB0_729
	s_waitcnt lgkmcnt(0)
	ds_read_b128 v[162:165], v219 offset:49248
	ds_read_b128 v[170:173], v219 offset:49216
	ds_read_b128 v[174:177], v219 offset:49184
	ds_read_b128 v[178:181], v219 offset:49152
	s_waitcnt lgkmcnt(3)
	s_nop 0
	v_pk_mul_f32 v[30:31], v[30:31], v[164:165]
	s_waitcnt lgkmcnt(2)
	s_nop 0
	v_pk_mul_f32 v[26:27], v[26:27], v[172:173]
	s_waitcnt lgkmcnt(1)
	s_nop 0
	v_pk_mul_f32 v[22:23], v[22:23], v[176:177]
	s_waitcnt lgkmcnt(0)
	s_nop 0
	v_pk_mul_f32 v[18:19], v[18:19], v[180:181]
	v_pk_mul_f32 v[28:29], v[28:29], v[162:163]
	v_pk_mul_f32 v[24:25], v[24:25], v[170:171]
	v_pk_mul_f32 v[20:21], v[20:21], v[174:175]
	v_pk_mul_f32 v[16:17], v[16:17], v[178:179]
	v_pk_mul_f32 v[14:15], v[14:15], v[164:165]
	v_pk_mul_f32 v[10:11], v[10:11], v[172:173]
	v_pk_mul_f32 v[6:7], v[6:7], v[176:177]
	v_pk_mul_f32 v[2:3], v[2:3], v[180:181]
	v_pk_mul_f32 v[12:13], v[12:13], v[162:163]
	v_pk_mul_f32 v[8:9], v[8:9], v[170:171]
	v_pk_mul_f32 v[4:5], v[4:5], v[174:175]
	v_pk_mul_f32 v[0:1], v[0:1], v[178:179]
.LBB0_729:
	s_add_i32 s18, s22, 0x2000
	v_add_u32_e64 v162, s38, v239
	s_cmpk_lg_i32 s22, 0x4000
	s_cselect_b32 s38, s18, 0
	s_add_i32 s18, s22, s30
	s_mov_b32 s19, m0
	s_mov_b32 m0, s18
	s_nop 0
	global_load_lds_dwordx4 v244, s[98:99]
	s_mov_b32 m0, s19
	s_add_i32 s18, s38, s31
	s_mov_b32 s19, m0
	s_mov_b32 m0, s18
	s_nop 0
	s_nop 0
	global_load_lds_dwordx4 v245, s[98:99]
	s_mov_b32 m0, s19
	s_nop 0
	s_add_u32 s98, s98, 0x20000
	s_addc_u32 s99, s99, 0
	s_nop 0
	ds_read_b64_tr_b16 v[194:195], v162 offset:24576
	ds_read_b64_tr_b16 v[196:197], v162 offset:25088
	s_waitcnt lgkmcnt(2)
	s_nop 0
	v_mfma_f32_32x32x16_bf16 v[80:95], v[134:137], v[110:113], v[80:95]
	v_add_f32_e32 v114, v48, v49
	v_add_f32_e32 v114, v50, v114
	v_add_f32_e32 v114, v51, v114
	v_add_f32_e32 v114, v52, v114
	v_add_f32_e64 v114, v53, v114
	v_cvt_pk_bf16_f32 v126, v48, v49
	v_cvt_pk_bf16_f32 v127, v50, v51
	ds_read_b64_tr_b16 v[190:191], v162 offset:28672
	ds_read_b64_tr_b16 v[192:193], v162 offset:29184
	v_mfma_f32_32x32x16_bf16 v[64:79], v[130:133], v[110:113], v[64:79]
	v_add_f32_e32 v48, v54, v114
	v_add_f32_e32 v48, v55, v48
	v_add_f32_e32 v48, v56, v48
	v_add_f32_e32 v48, v57, v48
	v_cvt_pk_bf16_f32 v128, v52, v53
	v_cvt_pk_bf16_f32 v129, v54, v55
	ds_read_b64_tr_b16 v[186:187], v162 offset:25600
	ds_read_b64_tr_b16 v[188:189], v162 offset:26112
	v_mfma_f32_32x32x16_bf16 v[80:95], v[146:149], v[106:109], v[80:95]
	v_add_f32_e32 v48, v58, v48
	v_add_f32_e32 v48, v59, v48
	v_add_f32_e32 v48, v60, v48
	v_add_f32_e32 v48, v61, v48
	v_cvt_pk_bf16_f32 v122, v56, v57
	v_cvt_pk_bf16_f32 v123, v58, v59
	ds_read_b64_tr_b16 v[138:139], v162 offset:29696
	ds_read_b64_tr_b16 v[140:141], v162 offset:30208
	v_mfma_f32_32x32x16_bf16 v[64:79], v[142:145], v[106:109], v[64:79]
	v_add_f32_e32 v48, v62, v48
	v_add_f32_e32 v48, v63, v48
	v_add_f32_e32 v48, v32, v48
	v_add_f32_e32 v48, v33, v48
	v_cvt_pk_bf16_f32 v124, v60, v61
	v_cvt_pk_bf16_f32 v125, v62, v63
	ds_read_b64_tr_b16 v[182:183], v162 offset:26624
	ds_read_b64_tr_b16 v[184:185], v162 offset:27136
	v_mfma_f32_32x32x16_bf16 v[80:95], v[158:161], v[102:105], v[80:95]
	v_add_f32_e32 v48, v34, v48
	v_add_f32_e32 v48, v35, v48
	v_add_f32_e32 v48, v36, v48
	v_add_f32_e32 v48, v37, v48
	v_cvt_pk_bf16_f32 v118, v32, v33
	v_cvt_pk_bf16_f32 v119, v34, v35
	ds_read_b64_tr_b16 v[178:179], v162 offset:30720
	ds_read_b64_tr_b16 v[180:181], v162 offset:31232
	v_mfma_f32_32x32x16_bf16 v[64:79], v[154:157], v[102:105], v[64:79]
	v_add_f32_e32 v32, v38, v48
	v_add_f32_e32 v32, v39, v32
	v_add_f32_e32 v32, v40, v32
	v_add_f32_e32 v32, v41, v32
	v_cvt_pk_bf16_f32 v120, v36, v37
	v_cvt_pk_bf16_f32 v121, v38, v39
	ds_read_b64_tr_b16 v[174:175], v162 offset:27648
	ds_read_b64_tr_b16 v[176:177], v162 offset:28160
	v_mfma_f32_32x32x16_bf16 v[80:95], v[166:169], v[98:101], v[80:95]
	v_add_f32_e32 v32, v42, v32
	v_add_f32_e32 v32, v43, v32
	v_add_f32_e32 v32, v44, v32
	v_add_f32_e32 v32, v45, v32
	v_cvt_pk_bf16_f32 v114, v40, v41
	v_cvt_pk_bf16_f32 v115, v42, v43
	ds_read_b64_tr_b16 v[170:171], v162 offset:31744
	ds_read_b64_tr_b16 v[172:173], v162 offset:32256
	v_mfma_f32_32x32x16_bf16 v[64:79], v[150:153], v[98:101], v[64:79]
	v_add_f32_e32 v32, v46, v32
	v_add_f32_e32 v32, v47, v32
	v_add_f32_e64 v240, v224, v32
	v_cvt_pk_bf16_f32 v116, v44, v45
	v_cvt_pk_bf16_f32 v117, v46, v47
	s_waitcnt lgkmcnt(14)
	s_nop 0
	ds_read_b128 v[32:35], v205 offset:256
	ds_read_b128 v[36:39], v205 offset:288
	ds_read_b128 v[50:53], v205 offset:384
	ds_read_b128 v[54:57], v205 offset:416
	ds_read_b128 v[40:43], v205 offset:320
	ds_read_b128 v[44:47], v205 offset:352
	ds_read_b128 v[58:61], v205 offset:448
	ds_read_b128 v[162:165], v205 offset:480
	v_max_f32_e64 v48, v80, v81
	v_max3_f32 v49, v82, v83, v65
	v_max3_f32 v48, v48, v64, v66
	v_max3_f32 v48, v48, v67, v84
	v_max3_f32 v49, v49, v86, v87
	v_max3_f32 v48, v48, v85, v68
	v_max3_f32 v49, v49, v70, v71
	v_max3_f32 v48, v48, v69, v88
	v_max3_f32 v49, v49, v90, v91
	v_max3_f32 v48, v48, v89, v72
	v_max3_f32 v49, v49, v74, v75
	v_max3_f32 v48, v48, v73, v92
	v_max3_f32 v49, v49, v94, v95
	v_max3_f32 v48, v48, v93, v76
	v_max3_f32 v49, v49, v78, v79
	v_max3_f32 v48, v48, v77, v49
	v_mov_b32_e32 v49, v48
	s_nop 1
	v_permlane32_swap_b32_e32 v48, v49
	v_max_f32_e32 v48, v48, v49
	v_cmp_lt_f32_e32 vcc, s51, v48
	s_cmp_lg_u64 vcc, 0
	s_cselect_b64 s[18:19], -1, 0
	s_cbranch_vccnz .LBB0_737
.LBB0_730:
	v_mfma_f32_32x32x16_bf16 v[16:31], v[126:129], v[194:197], v[16:31]
	v_exp_f32_e32 v80, v80
	v_exp_f32_e32 v81, v81
	v_exp_f32_e64 v82, v82
	v_exp_f32_e32 v83, v83
	s_waitcnt lgkmcnt(14)
	v_mfma_f32_32x32x16_bf16 v[0:15], v[126:129], v[190:193], v[0:15]
	v_exp_f32_e32 v84, v84
	v_exp_f32_e32 v85, v85
	v_exp_f32_e32 v86, v86
	v_exp_f32_e32 v87, v87
	v_add_u32_e64 v48, s38, v238
	ds_read_b128 v[158:161], v48
	ds_read_b128 v[146:149], v48 offset:512
	v_mfma_f32_32x32x16_bf16 v[16:31], v[122:125], v[186:189], v[16:31]
	v_exp_f32_e32 v88, v88
	v_exp_f32_e32 v89, v89
	v_exp_f32_e32 v90, v90
	v_exp_f32_e32 v91, v91
	ds_read_b128 v[154:157], v48 offset:2048
	ds_read_b128 v[142:145], v48 offset:2560
	v_mfma_f32_32x32x16_bf16 v[0:15], v[122:125], v[138:141], v[0:15]
	v_exp_f32_e32 v92, v92
	v_exp_f32_e32 v93, v93
	v_exp_f32_e32 v94, v94
	v_exp_f32_e32 v95, v95
	ds_read_b128 v[150:153], v48 offset:4096
	ds_read_b128 v[138:141], v48 offset:4608
	v_mfma_f32_32x32x16_bf16 v[16:31], v[118:121], v[182:185], v[16:31]
	v_exp_f32_e32 v64, v64
	v_exp_f32_e32 v65, v65
	v_exp_f32_e32 v66, v66
	v_exp_f32_e32 v67, v67
	ds_read_b128 v[134:137], v48 offset:6144
	ds_read_b128 v[130:133], v48 offset:6656
	s_waitcnt lgkmcnt(14)
	s_nop 0
	v_mfma_f32_32x32x16_bf16 v[0:15], v[118:121], v[178:181], v[0:15]
	v_exp_f32_e32 v68, v68
	v_exp_f32_e32 v69, v69
	v_exp_f32_e32 v70, v70
	v_exp_f32_e32 v71, v71
	v_mfma_f32_32x32x16_bf16 v[16:31], v[114:117], v[174:177], v[16:31]
	v_exp_f32_e32 v72, v72
	v_exp_f32_e32 v73, v73
	v_exp_f32_e32 v74, v74
	v_exp_f32_e32 v75, v75
	v_mfma_f32_32x32x16_bf16 v[0:15], v[114:117], v[170:173], v[0:15]
	v_exp_f32_e32 v76, v76
	v_exp_f32_e32 v77, v77
	v_exp_f32_e64 v78, v78
	v_exp_f32_e32 v79, v79
	s_waitcnt vmcnt(2) lgkmcnt(0)
	v_pk_add_f32 v[48:49], v[32:33], v[202:203] op_sel_hi:[1,0] neg_lo:[0,1] neg_hi:[0,1]
	v_pk_add_f32 v[32:33], v[50:51], v[202:203] op_sel_hi:[1,0] neg_lo:[0,1] neg_hi:[0,1]
	v_pk_add_f32 v[50:51], v[34:35], v[202:203] op_sel_hi:[1,0] neg_lo:[0,1] neg_hi:[0,1]
	v_pk_add_f32 v[34:35], v[52:53], v[202:203] op_sel_hi:[1,0] neg_lo:[0,1] neg_hi:[0,1]
	v_pk_add_f32 v[52:53], v[36:37], v[202:203] op_sel_hi:[1,0] neg_lo:[0,1] neg_hi:[0,1]
	v_pk_add_f32 v[36:37], v[54:55], v[202:203] op_sel_hi:[1,0] neg_lo:[0,1] neg_hi:[0,1]
	v_pk_add_f32 v[54:55], v[38:39], v[202:203] op_sel_hi:[1,0] neg_lo:[0,1] neg_hi:[0,1]
	v_pk_add_f32 v[38:39], v[56:57], v[202:203] op_sel_hi:[1,0] neg_lo:[0,1] neg_hi:[0,1]
	v_pk_add_f32 v[56:57], v[40:41], v[202:203] op_sel_hi:[1,0] neg_lo:[0,1] neg_hi:[0,1]
	v_pk_add_f32 v[40:41], v[58:59], v[202:203] op_sel_hi:[1,0] neg_lo:[0,1] neg_hi:[0,1]
	v_pk_add_f32 v[58:59], v[42:43], v[202:203] op_sel_hi:[1,0] neg_lo:[0,1] neg_hi:[0,1]
	v_pk_add_f32 v[42:43], v[60:61], v[202:203] op_sel_hi:[1,0] neg_lo:[0,1] neg_hi:[0,1]
	v_pk_add_f32 v[60:61], v[44:45], v[202:203] op_sel_hi:[1,0] neg_lo:[0,1] neg_hi:[0,1]
	v_pk_add_f32 v[44:45], v[162:163], v[202:203] op_sel_hi:[1,0] neg_lo:[0,1] neg_hi:[0,1]
	v_pk_add_f32 v[62:63], v[46:47], v[202:203] op_sel_hi:[1,0] neg_lo:[0,1] neg_hi:[0,1]
	v_pk_add_f32 v[46:47], v[164:165], v[202:203] op_sel_hi:[1,0] neg_lo:[0,1] neg_hi:[0,1]
	s_barrier
	s_andn2_b64 vcc, exec, s[18:19]
	s_cbranch_vccnz .LBB0_732
	s_waitcnt lgkmcnt(0)
	ds_read_b128 v[166:169], v219 offset:49248
	ds_read_b128 v[170:173], v219 offset:49216
	ds_read_b128 v[174:177], v219 offset:49184
	ds_read_b128 v[178:181], v219 offset:49152
	s_waitcnt lgkmcnt(3)
	s_nop 0
	v_pk_mul_f32 v[30:31], v[30:31], v[168:169]
	s_waitcnt lgkmcnt(2)
	s_nop 0
	v_pk_mul_f32 v[26:27], v[26:27], v[172:173]
	s_waitcnt lgkmcnt(1)
	s_nop 0
	v_pk_mul_f32 v[22:23], v[22:23], v[176:177]
	s_waitcnt lgkmcnt(0)
	s_nop 0
	v_pk_mul_f32 v[18:19], v[18:19], v[180:181]
	v_pk_mul_f32 v[28:29], v[28:29], v[166:167]
	v_pk_mul_f32 v[24:25], v[24:25], v[170:171]
	v_pk_mul_f32 v[20:21], v[20:21], v[174:175]
	v_pk_mul_f32 v[16:17], v[16:17], v[178:179]
	v_pk_mul_f32 v[14:15], v[14:15], v[168:169]
	v_pk_mul_f32 v[10:11], v[10:11], v[172:173]
	v_pk_mul_f32 v[6:7], v[6:7], v[176:177]
	v_pk_mul_f32 v[2:3], v[2:3], v[180:181]
	v_pk_mul_f32 v[12:13], v[12:13], v[166:167]
	v_pk_mul_f32 v[8:9], v[8:9], v[170:171]
	v_pk_mul_f32 v[4:5], v[4:5], v[174:175]
	v_pk_mul_f32 v[0:1], v[0:1], v[178:179]
.LBB0_732:
	s_add_i32 s18, s38, 0x2000
	s_cmpk_lg_i32 s38, 0x4000
	s_cselect_b32 s46, s18, 0
	s_add_i32 s18, s23, 2
	s_nop 0
	s_mov_b64 s[20:21], 0x40000
	v_lshl_add_u64 v[206:207], v[206:207], 0, s[20:21]
	s_mov_b64 s[62:63], 0x40000
	v_lshl_add_u64 v[208:209], v[208:209], 0, s[20:21]
	s_cmp_ge_u32 s18, s39
	s_nop 0
	v_add_u32_e32 v205, 0x200, v205
	s_cbranch_scc1 .LBB0_749
	s_mov_b32 s23, s18
	s_mov_b32 s18, s22
	s_mov_b32 s22, s46
	s_branch .LBB0_726
.LBB0_734:
	v_max_f32_e32 v80, v80, v80
	v_max_f32_e64 v81, 0, v80
	v_exp_f32_e64 v80, -v81
	s_and_saveexec_b64 s[20:21], s[2:3]
	s_nop 0
	ds_write_b32 v235, v80 offset:49152
	s_or_b64 exec, exec, s[20:21]
	v_sub_f32_e32 v63, v63, v81
	v_sub_f32_e32 v62, v62, v81
	v_sub_f32_e32 v61, v61, v81
	v_sub_f32_e32 v60, v60, v81
	v_sub_f32_e32 v59, v59, v81
	v_sub_f32_e32 v58, v58, v81
	v_sub_f32_e32 v57, v57, v81
	v_sub_f32_e32 v56, v56, v81
	v_sub_f32_e32 v55, v55, v81
	v_sub_f32_e32 v54, v54, v81
	v_sub_f32_e32 v53, v53, v81
	v_sub_f32_e32 v52, v52, v81
	v_sub_f32_e32 v51, v51, v81
	v_sub_f32_e32 v50, v50, v81
	v_sub_f32_e32 v49, v49, v81
	v_sub_f32_e32 v48, v48, v81
	v_sub_f32_e32 v47, v47, v81
	v_sub_f32_e32 v46, v46, v81
	v_sub_f32_e32 v45, v45, v81
	v_sub_f32_e32 v44, v44, v81
	v_sub_f32_e32 v43, v43, v81
	v_sub_f32_e32 v42, v42, v81
	v_sub_f32_e32 v41, v41, v81
	v_sub_f32_e32 v40, v40, v81
	v_sub_f32_e32 v39, v39, v81
	v_sub_f32_e32 v38, v38, v81
	v_sub_f32_e32 v37, v37, v81
	v_sub_f32_e32 v36, v36, v81
	v_sub_f32_e32 v35, v35, v81
	v_sub_f32_e32 v34, v34, v81
	v_sub_f32_e32 v33, v33, v81
	v_sub_f32_e32 v32, v32, v81
	v_add_f32_e32 v202, v202, v81
	v_mul_f32_e32 v224, v224, v80
	s_branch .LBB0_727
.LBB0_737:
	v_max_f32_e32 v48, v48, v48
	v_max_f32_e32 v49, 0, v48
	v_exp_f32_e64 v48, -v49
	s_and_saveexec_b64 s[20:21], s[2:3]
	s_nop 0
	ds_write_b32 v235, v48 offset:49152
	s_or_b64 exec, exec, s[20:21]
	v_sub_f32_e32 v95, v95, v49
	v_sub_f32_e32 v94, v94, v49
	v_sub_f32_e32 v93, v93, v49
	v_sub_f32_e32 v92, v92, v49
	v_sub_f32_e32 v91, v91, v49
	v_sub_f32_e32 v90, v90, v49
	v_sub_f32_e32 v89, v89, v49
	v_sub_f32_e32 v88, v88, v49
	v_sub_f32_e32 v87, v87, v49
	v_sub_f32_e32 v86, v86, v49
	v_sub_f32_e32 v85, v85, v49
	v_sub_f32_e32 v84, v84, v49
	v_sub_f32_e32 v83, v83, v49
	v_sub_f32_e32 v82, v82, v49
	v_sub_f32_e32 v81, v81, v49
	v_sub_f32_e32 v80, v80, v49
	v_sub_f32_e32 v79, v79, v49
	v_sub_f32_e32 v78, v78, v49
	v_sub_f32_e32 v77, v77, v49
	v_sub_f32_e32 v76, v76, v49
	v_sub_f32_e32 v75, v75, v49
	v_sub_f32_e32 v74, v74, v49
	v_sub_f32_e32 v73, v73, v49
	v_sub_f32_e32 v72, v72, v49
	v_sub_f32_e32 v71, v71, v49
	v_sub_f32_e32 v70, v70, v49
	v_sub_f32_e32 v69, v69, v49
	v_sub_f32_e32 v68, v68, v49
	v_sub_f32_e32 v67, v67, v49
	v_sub_f32_e32 v66, v66, v49
	v_sub_f32_e32 v65, v65, v49
	v_sub_f32_e32 v64, v64, v49
	v_add_f32_e32 v202, v202, v49
	v_mul_f32_e32 v240, v240, v48
	s_branch .LBB0_730
